# v5: P7 side job staged in VGPRs (two slots, loads in flight a whole loop body), K-loop vmcnt waits 8->11 in steady state
# speedup vs baseline: 1.0142x; 1.0142x over previous
.LBB0_765:
	s_lshl_b32 s53, s96, 7
	s_and_b32 s13, s12, 0xc0
	s_add_i32 s14, 0, 0x26000
	s_add_i32 s16, 0, 0x24000
	s_add_i32 s52, s53, -1
	s_add_u32 s4, s42, 0x84000
	s_addc_u32 s5, s43, 0
	s_add_i32 s17, 0, 0x18000
	s_add_i32 s10, s17, s3
	v_lshl_add_u64 v[6:7], s[4:5], 0, v[214:215]
	s_mov_b32 m0, s10
	s_waitcnt vmcnt(2)
	s_barrier
	global_load_lds_dwordx4 v[6:7], off
	s_add_i32 m0, s10, 0x2000
	s_add_i32 s54, s15, 0x8000
	s_add_i32 s55, s15, 0xa000
	v_lshl_add_u64 v[6:7], s[4:5], 0, v[218:219]
	s_mov_b64 s[10:11], 0x80
	s_add_u32 s4, s42, 0x85000
	global_load_lds_dwordx4 v[6:7], off
	v_lshl_add_u64 v[4:5], v[4:5], 0, s[10:11]
	s_mov_b32 m0, s54
	s_addc_u32 s5, s43, 0
	s_add_i32 s18, 0, 0x1c000
	global_load_lds_dwordx4 v[4:5], off
	v_lshl_add_u64 v[2:3], v[2:3], 0, s[10:11]
	s_mov_b32 m0, s55
	s_add_i32 s3, s18, s3
	global_load_lds_dwordx4 v[2:3], off
	v_lshl_add_u64 v[2:3], s[4:5], 0, v[214:215]
	s_mov_b32 m0, s3
	v_lshlrev_b32_e32 v4, 11, v205
	global_load_lds_dwordx4 v[2:3], off
	v_lshl_add_u64 v[2:3], s[4:5], 0, v[218:219]
	s_add_i32 m0, s3, 0x2000
	v_mov_b32_e32 v67, 0
	global_load_lds_dwordx4 v[2:3], off
	v_or_b32_e32 v3, s13, v211
	v_lshl_or_b32 v2, s2, 13, v222
	v_bitop3_b32 v3, v3, v221, v220 bitop3:0xde
	s_add_i32 s2, 0, 0x10000
	v_add_u32_e32 v228, s2, v3
	s_add_i32 s2, 0, 0x14000
	s_cmpk_lt_u32 s12, 0x100
	v_add_u32_e32 v229, s2, v3
	s_cselect_b64 s[12:13], -1, 0
	s_add_i32 s2, 0, 0x10008
	v_add_u32_e32 v232, s2, v3
	s_add_i32 s2, 0, 0x14008
	v_add_u32_e32 v233, s2, v3
	s_add_i32 s2, 0, 0x18008
	v_add_u32_e32 v234, s2, v3
	s_add_i32 s2, 0, 0x1c008
	v_add_u32_e32 v230, s17, v3
	v_add_u32_e32 v231, s18, v3
	v_add_u32_e32 v235, s2, v3
	v_lshlrev_b32_e32 v3, 8, v0
	v_and_b32_e32 v3, 0x18000, v3
	v_or3_b32 v3, v1, v3, v4
	v_add_u32_e32 v220, v3, v204
	v_lshlrev_b32_e32 v3, 4, v207
	v_and_b32_e32 v3, 0x38000, v3
	s_waitcnt vmcnt(6)
	v_or3_b32 v1, v1, v3, v4
	v_mov_b32_e32 v68, v67
	v_mov_b32_e32 v69, v67
	s_add_i32 s2, 0, 0x20480
	v_add_u32_e32 v222, v1, v204
	v_mov_b32_e32 v66, v67
	v_mov_b32_e32 v1, s2
	s_add_i32 s2, 0, 0x20504
	v_mov_b64_e32 v[72:73], v[68:69]
	v_mov_b64_e32 v[76:77], v[68:69]
	v_add_u32_e32 v227, s14, v209
	v_add_u32_e32 v209, s16, v209
	v_mov_b32_e32 v211, v67
	v_mov_b32_e32 v221, v67
	v_mov_b32_e32 v223, v67
	s_mov_b64 s[4:5], 0
	s_mov_b32 s98, -1
	s_mov_b32 s99, -1
	s_mov_b32 s100, 0
	v_mov_b32_e32 v207, s2
	s_mov_b32 s14, 0x42800000
	s_mov_b64 s[16:17], 0x2000
	s_mov_b32 s18, 0x3a800000
	s_mov_b32 s56, 0xc0e00000
	s_mov_b32 s57, 0xc3e00000
	v_add_u32_e32 v236, 0, v2
	v_mov_b32_e32 v237, 0x40e00000
	v_mov_b32_e32 v238, 0x43e00000
	v_mov_b64_e32 v[70:71], v[66:67]
	v_mov_b64_e32 v[74:75], v[66:67]
	s_mov_b32 s58, 0
	s_barrier

; #define PG8_LAS __attribute__((address_space(3)))
;     __device__ __forceinline__ void issue(PG8_LAS unsigned char* lds0, int j, int tid, int wid) const {
;         const float* s0; unsigned char* d; addr(j, tid, s0, d);
;         __builtin_amdgcn_global_load_lds((const unsigned*)s0, (PG8_LAS unsigned*)(lds0 + stage + wid * 1024), 16, 0, 2);
;         __builtin_amdgcn_global_load_lds((const unsigned*)(s0 + ntot), (PG8_LAS unsigned*)(lds0 + stage + 8192 + wid * 1024), 16, 0, 2);
;     }
;     __device__ __forceinline__ void read(v4i_t& t0, v4i_t& t1, int tid, unsigned ldsb) const {
;         asm volatile("ds_read_b128 %0, %1" : "=&v"(t0) : "v"(ldsb + stage + 16u * (unsigned)tid) : "memory");
;         asm volatile("ds_read_b128 %0, %1" : "=&v"(t1) : "v"(ldsb + stage + 8192u + 16u * (unsigned)tid) : "memory");
;     }
;     __device__ __forceinline__ void finish(v4i_t& t0, v4i_t& t1, int j, int tid) const {
;         asm volatile("" : "+v"(t0), "+v"(t1));
;         const float* s0; unsigned char* d; addr(j, tid, s0, d);
;         const f32x4 r0 = __builtin_bit_cast(f32x4, t0) * 64.f, r1 = __builtin_bit_cast(f32x4, t1) * 64.f;
;         int w0 = 0, w1 = 0; w0 = __builtin_amdgcn_cvt_pk_fp8_f32(r0[0], r1[0], w0, false); w0 = __builtin_amdgcn_cvt_pk_fp8_f32(r0[1], r1[1], w0, true);
;         w1 = __builtin_amdgcn_cvt_pk_fp8_f32(r0[2], r1[2], w1, false); w1 = __builtin_amdgcn_cvt_pk_fp8_f32(r0[3], r1[3], w1, true);
;         typedef int v2is __attribute__((ext_vector_type(2))); __builtin_nontemporal_store((v2is){w0, w1}, (v2is*)d);
.LBB0_782:
	ds_read_b64_tr_b16 v[26:27], v228 offset:0
	ds_read_b64_tr_b16 v[28:29], v228 offset:1024
	ds_read_b64_tr_b16 v[30:31], v228 offset:8192
	ds_read_b64_tr_b16 v[32:33], v228 offset:9216
	ds_read_b64_tr_b16 v[18:19], v232 offset:0
	ds_read_b64_tr_b16 v[20:21], v232 offset:1024
	ds_read_b64_tr_b16 v[22:23], v232 offset:8192
	ds_read_b64_tr_b16 v[24:25], v232 offset:9216
	ds_read_b64_tr_b16 v[10:11], v229 offset:0
	ds_read_b64_tr_b16 v[12:13], v229 offset:1024
	ds_read_b64_tr_b16 v[14:15], v229 offset:8192
	ds_read_b64_tr_b16 v[16:17], v229 offset:9216
	ds_read_b64_tr_b16 v[2:3], v233 offset:0
	ds_read_b64_tr_b16 v[4:5], v233 offset:1024
	ds_read_b64_tr_b16 v[6:7], v233 offset:8192
	ds_read_b64_tr_b16 v[8:9], v233 offset:9216
	v_lshl_add_u64 v[68:69], s[42:43], 0, v[220:221]
	s_add_i32 m0, s15, 0xc000
	s_waitcnt lgkmcnt(0)
	ds_read_b128 v[58:61], v236
	ds_read_b128 v[62:65], v236 offset:1024
	ds_read_b128 v[50:53], v236 offset:2048
	ds_read_b128 v[54:57], v236 offset:3072
	ds_read_b128 v[42:45], v236 offset:4096
	ds_read_b128 v[46:49], v236 offset:5120
	ds_read_b128 v[34:37], v236 offset:6144
	ds_read_b128 v[38:41], v236 offset:7168
	global_load_lds_dwordx4 v[68:69], off
	v_lshl_add_u64 v[68:69], s[42:43], 0, v[222:223]
	s_add_i32 m0, s15, 0xe000
	s_nop 0
	global_load_lds_dwordx4 v[68:69], off
	s_cmp_eq_u32 s100, 3
	s_cbranch_scc1 .Lp7vg_w11_a1
	s_waitcnt vmcnt(8)
	s_branch .Lp7vg_wd_a1
.Lp7vg_w11_a1:
	s_waitcnt vmcnt(11)
.Lp7vg_wd_a1:
	s_waitcnt lgkmcnt(0)
	s_mov_b32 s100, 0
	s_cmp_lt_i32 s98, 0
	s_cbranch_scc1 .Lp7vg_nf_a
	s_add_i32 s4, s98, s52
	s_add_i32 s4, s4, 1
	v_pk_mul_f32 v[70:71], v[70:71], s[14:15] op_sel_hi:[1,0]
	v_pk_mul_f32 v[72:73], v[72:73], s[14:15] op_sel_hi:[1,0]
	v_pk_mul_f32 v[74:75], v[74:75], s[14:15] op_sel_hi:[1,0]
	v_pk_mul_f32 v[76:77], v[76:77], s[14:15] op_sel_hi:[1,0]
	s_ashr_i32 s2, s4, 10
	s_ashr_i32 s3, s2, 31
	v_cvt_pk_fp8_f32 v70, v70, v74
	s_lshl_b32 s4, s4, 12
	s_lshl_b64 s[2:3], s[2:3], 22
	v_cvt_pk_fp8_f32 v70, v71, v75 op_sel:[0,0,1]
	s_and_b32 s4, s4, 0x3ff000
	v_readlane_b32 s5, v251, 50
	v_cvt_pk_fp8_f32 v71, v72, v76
	s_add_u32 s2, s5, s2
	v_readlane_b32 s5, v251, 51
	s_addc_u32 s3, s5, s3
	v_cvt_pk_fp8_f32 v71, v73, v77 op_sel:[0,0,1]
	s_add_u32 s2, s2, s4
	s_addc_u32 s3, s3, 0
	v_lshl_add_u64 v[68:69], s[2:3], 0, v[210:211]
	global_store_dwordx2 v[68:69], v[70:71], off nt
	s_mov_b32 s100, 1
.Lp7vg_nf_a:
	s_mov_b32 s98, -1
	s_cmpk_gt_i32 s48, 0x7f
	s_cbranch_scc1 .Lp7vg_ni_a
	s_add_i32 s4, s48, s53
	s_ashr_i32 s2, s4, 10
	s_ashr_i32 s3, s2, 31
	s_lshl_b64 s[2:3], s[2:3], 24
	s_lshl_b32 s4, s4, 14
	s_and_b32 s4, s4, 0xffc000
	s_add_u32 s2, s76, s2
	s_addc_u32 s3, s77, s3
	s_add_u32 s2, s2, s4
	s_addc_u32 s3, s3, 0
	v_lshlrev_b32_e32 v66, 2, v208
	v_lshl_add_u64 v[68:69], s[2:3], 0, v[66:67]
	v_lshl_add_u64 v[68:69], v[68:69], 0, s[16:17]
	global_load_dwordx4 v[70:73], v66, s[2:3] nt
	global_load_dwordx4 v[74:77], v[68:69], off nt
	s_mov_b32 s98, s48
	s_add_i32 s48, s48, 1
	s_add_i32 s100, s100, 2
.Lp7vg_ni_a:
	s_add_u32 s2, s42, 0xfffc0080
	s_addc_u32 s3, s43, -1
	s_cmp_eq_u32 s64, 12
	s_cselect_b32 s5, s23, s3
	s_cselect_b32 s4, s25, s2
	s_cselect_b32 s45, s35, s63
	s_cselect_b32 s44, s61, s62
	s_barrier
	s_setprio 1
	s_waitcnt lgkmcnt(0)
	v_mfma_scale_f32_16x16x128_f8f6f4 v[202:205], v[26:33], v[58:65], v[202:205], v226, v226 op_sel_hi:[0,0,0]
	v_mfma_scale_f32_16x16x128_f8f6f4 v[198:201], v[18:25], v[58:65], v[198:201], v226, v226 op_sel_hi:[0,0,0]
	v_mfma_scale_f32_16x16x128_f8f6f4 v[186:189], v[26:33], v[50:57], v[186:189], v226, v226 op_sel_hi:[0,0,0]
	v_mfma_scale_f32_16x16x128_f8f6f4 v[182:185], v[18:25], v[50:57], v[182:185], v226, v226 op_sel_hi:[0,0,0]
	v_mfma_scale_f32_16x16x128_f8f6f4 v[170:173], v[26:33], v[42:49], v[170:173], v226, v226 op_sel_hi:[0,0,0]
	v_mfma_scale_f32_16x16x128_f8f6f4 v[166:169], v[18:25], v[42:49], v[166:169], v226, v226 op_sel_hi:[0,0,0]
	v_mfma_scale_f32_16x16x128_f8f6f4 v[154:157], v[26:33], v[34:41], v[154:157], v226, v226 op_sel_hi:[0,0,0]
	v_mfma_scale_f32_16x16x128_f8f6f4 v[150:153], v[18:25], v[34:41], v[150:153], v226, v226 op_sel_hi:[0,0,0]
	s_setprio 0
	s_setprio 1
	v_mfma_scale_f32_16x16x128_f8f6f4 v[194:197], v[10:17], v[58:65], v[194:197], v226, v226 op_sel_hi:[0,0,0]
	v_mfma_scale_f32_16x16x128_f8f6f4 v[190:193], v[2:9], v[58:65], v[190:193], v226, v226 op_sel_hi:[0,0,0]
	v_mfma_scale_f32_16x16x128_f8f6f4 v[178:181], v[10:17], v[50:57], v[178:181], v226, v226 op_sel_hi:[0,0,0]
	v_mfma_scale_f32_16x16x128_f8f6f4 v[174:177], v[2:9], v[50:57], v[174:177], v226, v226 op_sel_hi:[0,0,0]
	v_mfma_scale_f32_16x16x128_f8f6f4 v[162:165], v[10:17], v[42:49], v[162:165], v226, v226 op_sel_hi:[0,0,0]
	v_mfma_scale_f32_16x16x128_f8f6f4 v[158:161], v[2:9], v[42:49], v[158:161], v226, v226 op_sel_hi:[0,0,0]
	v_mfma_scale_f32_16x16x128_f8f6f4 v[146:149], v[10:17], v[34:41], v[146:149], v226, v226 op_sel_hi:[0,0,0]
	v_mfma_scale_f32_16x16x128_f8f6f4 v[142:145], v[2:9], v[34:41], v[142:145], v226, v226 op_sel_hi:[0,0,0]
	s_setprio 0
	s_barrier
	s_mov_b32 m0, s19
	v_lshl_add_u64 v[68:69], s[44:45], 0, v[214:215]
	s_add_u32 s2, s44, 0x1000
	ds_read_b128 v[58:61], v236 offset:16384
	ds_read_b128 v[62:65], v236 offset:17408
	ds_read_b128 v[50:53], v236 offset:18432
	ds_read_b128 v[54:57], v236 offset:19456
	ds_read_b128 v[42:45], v236 offset:20480
	ds_read_b128 v[46:49], v236 offset:21504
	ds_read_b128 v[34:37], v236 offset:22528
	ds_read_b128 v[38:41], v236 offset:23552
	global_load_lds_dwordx4 v[68:69], off
	v_lshl_add_u64 v[68:69], s[44:45], 0, v[218:219]
	s_mov_b32 m0, s33
	s_addc_u32 s3, s45, 0
	global_load_lds_dwordx4 v[68:69], off
	v_lshl_add_u64 v[68:69], s[2:3], 0, v[214:215]
	s_mov_b32 m0, s37
	v_lshl_add_u64 v[224:225], s[4:5], 0, v[216:217]
	global_load_lds_dwordx4 v[68:69], off
	v_lshl_add_u64 v[68:69], s[2:3], 0, v[218:219]
	s_mov_b32 m0, s39
	v_cndmask_b32_e64 v66, 0, 1, s[40:41]
	global_load_lds_dwordx4 v[68:69], off
	v_lshl_add_u64 v[68:69], s[4:5], 0, v[212:213]
	s_mov_b32 m0, s15
	v_cmp_ne_u32_e64 s[2:3], 1, v66
	global_load_lds_dwordx4 v[68:69], off
	s_mov_b32 m0, s49
	s_andn2_b64 vcc, exec, s[40:41]
	global_load_lds_dwordx4 v[224:225], off
	s_cmp_eq_u32 s100, 3
	s_cbranch_scc1 .Lp7vg_w11_a2
	s_waitcnt vmcnt(8)
	s_branch .Lp7vg_wd_a2

.Lp7vg_wd_a2:
	s_waitcnt lgkmcnt(0)
	s_barrier
	s_cbranch_vccnz .LBB0_790
	s_setprio 1
	s_waitcnt lgkmcnt(0)
	v_mfma_scale_f32_16x16x128_f8f6f4 v[138:141], v[26:33], v[58:65], v[138:141], v226, v226 op_sel_hi:[0,0,0]
	v_mfma_scale_f32_16x16x128_f8f6f4 v[134:137], v[18:25], v[58:65], v[134:137], v226, v226 op_sel_hi:[0,0,0]
	v_mfma_scale_f32_16x16x128_f8f6f4 v[122:125], v[26:33], v[50:57], v[122:125], v226, v226 op_sel_hi:[0,0,0]
	v_mfma_scale_f32_16x16x128_f8f6f4 v[118:121], v[18:25], v[50:57], v[118:121], v226, v226 op_sel_hi:[0,0,0]
	v_mfma_scale_f32_16x16x128_f8f6f4 v[106:109], v[26:33], v[42:49], v[106:109], v226, v226 op_sel_hi:[0,0,0]
	v_mfma_scale_f32_16x16x128_f8f6f4 v[102:105], v[18:25], v[42:49], v[102:105], v226, v226 op_sel_hi:[0,0,0]
	v_mfma_scale_f32_16x16x128_f8f6f4 v[90:93], v[26:33], v[34:41], v[90:93], v226, v226 op_sel_hi:[0,0,0]
	v_mfma_scale_f32_16x16x128_f8f6f4 v[86:89], v[18:25], v[34:41], v[86:89], v226, v226 op_sel_hi:[0,0,0]
	s_setprio 0
	s_setprio 1
	v_mfma_scale_f32_16x16x128_f8f6f4 v[130:133], v[10:17], v[58:65], v[130:133], v226, v226 op_sel_hi:[0,0,0]
	v_mfma_scale_f32_16x16x128_f8f6f4 v[126:129], v[2:9], v[58:65], v[126:129], v226, v226 op_sel_hi:[0,0,0]
	v_mfma_scale_f32_16x16x128_f8f6f4 v[114:117], v[10:17], v[50:57], v[114:117], v226, v226 op_sel_hi:[0,0,0]
	v_mfma_scale_f32_16x16x128_f8f6f4 v[110:113], v[2:9], v[50:57], v[110:113], v226, v226 op_sel_hi:[0,0,0]
	v_mfma_scale_f32_16x16x128_f8f6f4 v[98:101], v[10:17], v[42:49], v[98:101], v226, v226 op_sel_hi:[0,0,0]
	v_mfma_scale_f32_16x16x128_f8f6f4 v[94:97], v[2:9], v[42:49], v[94:97], v226, v226 op_sel_hi:[0,0,0]
	v_mfma_scale_f32_16x16x128_f8f6f4 v[82:85], v[10:17], v[34:41], v[82:85], v226, v226 op_sel_hi:[0,0,0]
	v_mfma_scale_f32_16x16x128_f8f6f4 v[78:81], v[2:9], v[34:41], v[78:81], v226, v226 op_sel_hi:[0,0,0]
	s_setprio 0
.LBB0_790:
	s_barrier
	ds_read_b64_tr_b16 v[26:27], v230 offset:0
	ds_read_b64_tr_b16 v[28:29], v230 offset:1024
	ds_read_b64_tr_b16 v[30:31], v230 offset:8192
	ds_read_b64_tr_b16 v[32:33], v230 offset:9216
	ds_read_b64_tr_b16 v[18:19], v234 offset:0
	ds_read_b64_tr_b16 v[20:21], v234 offset:1024
	ds_read_b64_tr_b16 v[22:23], v234 offset:8192
	ds_read_b64_tr_b16 v[24:25], v234 offset:9216
	ds_read_b64_tr_b16 v[10:11], v231 offset:0
	ds_read_b64_tr_b16 v[12:13], v231 offset:1024
	ds_read_b64_tr_b16 v[14:15], v231 offset:8192
	ds_read_b64_tr_b16 v[16:17], v231 offset:9216
	ds_read_b64_tr_b16 v[2:3], v235 offset:0
	ds_read_b64_tr_b16 v[4:5], v235 offset:1024
	ds_read_b64_tr_b16 v[6:7], v235 offset:8192
	ds_read_b64_tr_b16 v[8:9], v235 offset:9216
	s_add_u32 s4, s4, 0x40000
	s_addc_u32 s5, s5, 0
	s_mov_b32 m0, s50
	v_lshl_add_u64 v[240:241], s[4:5], 0, v[212:213]
	s_waitcnt lgkmcnt(0)
	ds_read_b128 v[58:61], v236 offset:32768
	ds_read_b128 v[62:65], v236 offset:33792
	ds_read_b128 v[50:53], v236 offset:34816
	ds_read_b128 v[54:57], v236 offset:35840
	ds_read_b128 v[42:45], v236 offset:36864
	ds_read_b128 v[46:49], v236 offset:37888
	ds_read_b128 v[34:37], v236 offset:38912
	ds_read_b128 v[38:41], v236 offset:39936
	global_load_lds_dwordx4 v[240:241], off
	v_lshl_add_u64 v[240:241], s[4:5], 0, v[216:217]
	s_mov_b32 m0, s51
	s_nop 0
	global_load_lds_dwordx4 v[240:241], off
	s_cmp_eq_u32 s100, 3
	s_cbranch_scc1 .Lp7vg_w11_b1
	s_waitcnt vmcnt(8)
	s_branch .Lp7vg_wd_b1

; #define PG8_LAS __attribute__((address_space(3)))
;     __device__ __forceinline__ void issue(PG8_LAS unsigned char* lds0, int j, int tid, int wid) const {
;         const float* s0; unsigned char* d; addr(j, tid, s0, d);
;         __builtin_amdgcn_global_load_lds((const unsigned*)s0, (PG8_LAS unsigned*)(lds0 + stage + wid * 1024), 16, 0, 2);
;         __builtin_amdgcn_global_load_lds((const unsigned*)(s0 + ntot), (PG8_LAS unsigned*)(lds0 + stage + 8192 + wid * 1024), 16, 0, 2);
;     }
;     __device__ __forceinline__ void read(v4i_t& t0, v4i_t& t1, int tid, unsigned ldsb) const {
;         asm volatile("ds_read_b128 %0, %1" : "=&v"(t0) : "v"(ldsb + stage + 16u * (unsigned)tid) : "memory");
;         asm volatile("ds_read_b128 %0, %1" : "=&v"(t1) : "v"(ldsb + stage + 8192u + 16u * (unsigned)tid) : "memory");
;     }
;     __device__ __forceinline__ void finish(v4i_t& t0, v4i_t& t1, int j, int tid) const {
;         asm volatile("" : "+v"(t0), "+v"(t1));
;         const float* s0; unsigned char* d; addr(j, tid, s0, d);
;         const f32x4 r0 = __builtin_bit_cast(f32x4, t0) * 64.f, r1 = __builtin_bit_cast(f32x4, t1) * 64.f;
;         int w0 = 0, w1 = 0; w0 = __builtin_amdgcn_cvt_pk_fp8_f32(r0[0], r1[0], w0, false); w0 = __builtin_amdgcn_cvt_pk_fp8_f32(r0[1], r1[1], w0, true);
;         w1 = __builtin_amdgcn_cvt_pk_fp8_f32(r0[2], r1[2], w1, false); w1 = __builtin_amdgcn_cvt_pk_fp8_f32(r0[3], r1[3], w1, true);
;         typedef int v2is __attribute__((ext_vector_type(2))); __builtin_nontemporal_store((v2is){w0, w1}, (v2is*)d);
.Lp7vg_wd_b1:
	s_waitcnt lgkmcnt(0)
	s_mov_b32 s100, 0
	s_cmp_lt_i32 s99, 0
	s_cbranch_scc1 .Lp7vg_nf_b
	s_add_i32 s65, s99, s52
	s_add_i32 s65, s65, 1
	v_pk_mul_f32 v[242:243], v[242:243], s[14:15] op_sel_hi:[1,0]
	v_pk_mul_f32 v[244:245], v[244:245], s[14:15] op_sel_hi:[1,0]
	v_pk_mul_f32 v[246:247], v[246:247], s[14:15] op_sel_hi:[1,0]
	v_pk_mul_f32 v[248:249], v[248:249], s[14:15] op_sel_hi:[1,0]
	s_ashr_i32 s46, s65, 10
	s_ashr_i32 s47, s46, 31
	v_cvt_pk_fp8_f32 v242, v242, v246
	s_lshl_b32 s65, s65, 12
	s_lshl_b64 s[46:47], s[46:47], 22
	v_cvt_pk_fp8_f32 v242, v243, v247 op_sel:[0,0,1]
	s_and_b32 s65, s65, 0x3ff000
	v_readlane_b32 s4, v251, 50
	v_cvt_pk_fp8_f32 v243, v244, v248
	s_add_u32 s46, s4, s46
	v_readlane_b32 s4, v251, 51
	s_addc_u32 s47, s4, s47
	v_cvt_pk_fp8_f32 v243, v245, v249 op_sel:[0,0,1]
	s_add_u32 s46, s46, s65
	s_addc_u32 s47, s47, 0
	v_lshl_add_u64 v[240:241], s[46:47], 0, v[210:211]
	global_store_dwordx2 v[240:241], v[242:243], off nt
	s_mov_b32 s100, 1
.Lp7vg_nf_b:
	s_mov_b32 s99, -1
	s_cmpk_gt_i32 s48, 0x7f
	s_cbranch_scc1 .Lp7vg_ni_b
	s_add_i32 s65, s48, s53
	s_ashr_i32 s46, s65, 10
	s_ashr_i32 s47, s46, 31
	s_lshl_b64 s[46:47], s[46:47], 24
	s_lshl_b32 s65, s65, 14
	s_and_b32 s65, s65, 0xffc000
	s_add_u32 s46, s76, s46
	s_addc_u32 s47, s77, s47
	s_add_u32 s46, s46, s65
	s_addc_u32 s47, s47, 0
	v_lshlrev_b32_e32 v66, 2, v208
	v_lshl_add_u64 v[240:241], s[46:47], 0, v[66:67]
	v_lshl_add_u64 v[240:241], v[240:241], 0, s[16:17]
	global_load_dwordx4 v[242:245], v66, s[46:47] nt
	global_load_dwordx4 v[246:249], v[240:241], off nt
	s_mov_b32 s99, s48
	s_add_i32 s48, s48, 1
	s_add_i32 s100, s100, 2
.Lp7vg_ni_b:
	s_add_u32 s46, s44, 0x84000
	s_addc_u32 s47, s45, 0
	s_barrier
	s_setprio 1
	s_waitcnt lgkmcnt(0)
	v_mfma_scale_f32_16x16x128_f8f6f4 v[202:205], v[26:33], v[58:65], v[202:205], v226, v226 op_sel_hi:[0,0,0]
	v_mfma_scale_f32_16x16x128_f8f6f4 v[198:201], v[18:25], v[58:65], v[198:201], v226, v226 op_sel_hi:[0,0,0]
	v_mfma_scale_f32_16x16x128_f8f6f4 v[186:189], v[26:33], v[50:57], v[186:189], v226, v226 op_sel_hi:[0,0,0]
	v_mfma_scale_f32_16x16x128_f8f6f4 v[182:185], v[18:25], v[50:57], v[182:185], v226, v226 op_sel_hi:[0,0,0]
	v_mfma_scale_f32_16x16x128_f8f6f4 v[170:173], v[26:33], v[42:49], v[170:173], v226, v226 op_sel_hi:[0,0,0]
	v_mfma_scale_f32_16x16x128_f8f6f4 v[166:169], v[18:25], v[42:49], v[166:169], v226, v226 op_sel_hi:[0,0,0]
	v_mfma_scale_f32_16x16x128_f8f6f4 v[154:157], v[26:33], v[34:41], v[154:157], v226, v226 op_sel_hi:[0,0,0]
	v_mfma_scale_f32_16x16x128_f8f6f4 v[150:153], v[18:25], v[34:41], v[150:153], v226, v226 op_sel_hi:[0,0,0]
	s_setprio 0
	s_setprio 1
	v_mfma_scale_f32_16x16x128_f8f6f4 v[194:197], v[10:17], v[58:65], v[194:197], v226, v226 op_sel_hi:[0,0,0]
	v_mfma_scale_f32_16x16x128_f8f6f4 v[190:193], v[2:9], v[58:65], v[190:193], v226, v226 op_sel_hi:[0,0,0]
	v_mfma_scale_f32_16x16x128_f8f6f4 v[178:181], v[10:17], v[50:57], v[178:181], v226, v226 op_sel_hi:[0,0,0]
	v_mfma_scale_f32_16x16x128_f8f6f4 v[174:177], v[2:9], v[50:57], v[174:177], v226, v226 op_sel_hi:[0,0,0]
	v_mfma_scale_f32_16x16x128_f8f6f4 v[162:165], v[10:17], v[42:49], v[162:165], v226, v226 op_sel_hi:[0,0,0]
	v_mfma_scale_f32_16x16x128_f8f6f4 v[158:161], v[2:9], v[42:49], v[158:161], v226, v226 op_sel_hi:[0,0,0]
	v_mfma_scale_f32_16x16x128_f8f6f4 v[146:149], v[10:17], v[34:41], v[146:149], v226, v226 op_sel_hi:[0,0,0]
	v_mfma_scale_f32_16x16x128_f8f6f4 v[142:145], v[2:9], v[34:41], v[142:145], v226, v226 op_sel_hi:[0,0,0]
	s_setprio 0
	s_barrier
	v_lshl_add_u64 v[240:241], s[46:47], 0, v[214:215]
	s_add_i32 m0, s15, 0x18000
	ds_read_b128 v[58:61], v236 offset:49152
	ds_read_b128 v[62:65], v236 offset:50176
	ds_read_b128 v[50:53], v236 offset:51200
	ds_read_b128 v[54:57], v236 offset:52224
	ds_read_b128 v[42:45], v236 offset:53248
	ds_read_b128 v[46:49], v236 offset:54272
	ds_read_b128 v[34:37], v236 offset:55296
	ds_read_b128 v[38:41], v236 offset:56320
	global_load_lds_dwordx4 v[240:241], off
	s_add_i32 m0, s15, 0x1a000
	s_add_u32 s44, s44, 0x85000
	v_lshl_add_u64 v[240:241], s[46:47], 0, v[218:219]
	s_addc_u32 s45, s45, 0
	global_load_lds_dwordx4 v[240:241], off
	v_lshl_add_u64 v[240:241], s[44:45], 0, v[214:215]
	s_add_i32 m0, s15, 0x1c000
	v_lshl_add_u64 v[68:69], v[68:69], 0, s[10:11]
	global_load_lds_dwordx4 v[240:241], off
	v_lshl_add_u64 v[240:241], s[44:45], 0, v[218:219]
	s_add_i32 m0, s15, 0x1e000
	s_and_b64 vcc, exec, s[2:3]
	global_load_lds_dwordx4 v[240:241], off
	s_mov_b32 m0, s54
	s_nop 0
	global_load_lds_dwordx4 v[68:69], off
	v_lshl_add_u64 v[68:69], v[224:225], 0, s[10:11]
	s_mov_b32 m0, s55
	s_nop 0
	global_load_lds_dwordx4 v[68:69], off
	s_cmp_eq_u32 s100, 3
	s_cbranch_scc1 .Lp7vg_w11_b2
	s_waitcnt vmcnt(8)
	s_branch .Lp7vg_wd_b2

.Lp7vg_wd_b2:
	s_waitcnt lgkmcnt(0)
	s_barrier
	s_cbranch_vccnz .LBB0_781
	s_setprio 1
	s_waitcnt lgkmcnt(0)
	v_mfma_scale_f32_16x16x128_f8f6f4 v[138:141], v[26:33], v[58:65], v[138:141], v226, v226 op_sel_hi:[0,0,0]
	v_mfma_scale_f32_16x16x128_f8f6f4 v[134:137], v[18:25], v[58:65], v[134:137], v226, v226 op_sel_hi:[0,0,0]
	v_mfma_scale_f32_16x16x128_f8f6f4 v[122:125], v[26:33], v[50:57], v[122:125], v226, v226 op_sel_hi:[0,0,0]
	v_mfma_scale_f32_16x16x128_f8f6f4 v[118:121], v[18:25], v[50:57], v[118:121], v226, v226 op_sel_hi:[0,0,0]
	v_mfma_scale_f32_16x16x128_f8f6f4 v[106:109], v[26:33], v[42:49], v[106:109], v226, v226 op_sel_hi:[0,0,0]
	v_mfma_scale_f32_16x16x128_f8f6f4 v[102:105], v[18:25], v[42:49], v[102:105], v226, v226 op_sel_hi:[0,0,0]
	v_mfma_scale_f32_16x16x128_f8f6f4 v[90:93], v[26:33], v[34:41], v[90:93], v226, v226 op_sel_hi:[0,0,0]
	v_mfma_scale_f32_16x16x128_f8f6f4 v[86:89], v[18:25], v[34:41], v[86:89], v226, v226 op_sel_hi:[0,0,0]
	s_setprio 0
	s_setprio 1
	v_mfma_scale_f32_16x16x128_f8f6f4 v[130:133], v[10:17], v[58:65], v[130:133], v226, v226 op_sel_hi:[0,0,0]
	v_mfma_scale_f32_16x16x128_f8f6f4 v[126:129], v[2:9], v[58:65], v[126:129], v226, v226 op_sel_hi:[0,0,0]
	v_mfma_scale_f32_16x16x128_f8f6f4 v[114:117], v[10:17], v[50:57], v[114:117], v226, v226 op_sel_hi:[0,0,0]
	v_mfma_scale_f32_16x16x128_f8f6f4 v[110:113], v[2:9], v[50:57], v[110:113], v226, v226 op_sel_hi:[0,0,0]
	v_mfma_scale_f32_16x16x128_f8f6f4 v[98:101], v[10:17], v[42:49], v[98:101], v226, v226 op_sel_hi:[0,0,0]
	v_mfma_scale_f32_16x16x128_f8f6f4 v[94:97], v[2:9], v[42:49], v[94:97], v226, v226 op_sel_hi:[0,0,0]
	v_mfma_scale_f32_16x16x128_f8f6f4 v[82:85], v[10:17], v[34:41], v[82:85], v226, v226 op_sel_hi:[0,0,0]
	v_mfma_scale_f32_16x16x128_f8f6f4 v[78:81], v[2:9], v[34:41], v[78:81], v226, v226 op_sel_hi:[0,0,0]
	s_setprio 0
	s_branch .LBB0_781

; __device__ __forceinline__ void xcd_barrier(const XcdBarrier& b) {
;     asm volatile("s_waitcnt vmcnt(0)" ::: "memory");
;     __syncthreads();
;     if (threadIdx.x == 0) {
;         unsigned* bar = b.bar;
;         __builtin_amdgcn_s_waitcnt(0);
;         unsigned nloc = b.st[0], nx = b.st[1];
;         if (nloc == 0u) { xcd_barrier_complete(bar, b.x, nloc, nx); b.st[0] = nloc; b.st[1] = nx; }
.LBB0_808:
	s_waitcnt vmcnt(0)
	v_readlane_b32 s56, v251, 54
	v_readlane_b32 s29, v251, 19
	s_barrier
	v_readlane_b32 s57, v251, 55
	s_mov_b32 s2, 0x42800000
	s_cmp_lt_i32 s98, 0
	s_cbranch_scc1 .Lp7vg_dx
	s_add_i32 s0, s98, s52
	s_add_i32 s0, s0, 1
	v_pk_mul_f32 v[70:71], v[70:71], s[2:3] op_sel_hi:[1,0]
	v_pk_mul_f32 v[72:73], v[72:73], s[2:3] op_sel_hi:[1,0]
	v_pk_mul_f32 v[74:75], v[74:75], s[2:3] op_sel_hi:[1,0]
	v_pk_mul_f32 v[76:77], v[76:77], s[2:3] op_sel_hi:[1,0]
	s_ashr_i32 s4, s0, 10
	s_ashr_i32 s5, s4, 31
	v_cvt_pk_fp8_f32 v70, v70, v74
	s_lshl_b32 s0, s0, 12
	s_lshl_b64 s[4:5], s[4:5], 22
	v_cvt_pk_fp8_f32 v70, v71, v75 op_sel:[0,0,1]
	s_and_b32 s0, s0, 0x3ff000
	v_readlane_b32 s1, v251, 50
	v_cvt_pk_fp8_f32 v71, v72, v76
	s_add_u32 s4, s1, s4
	v_readlane_b32 s1, v251, 51
	s_addc_u32 s5, s1, s5
	v_cvt_pk_fp8_f32 v71, v73, v77 op_sel:[0,0,1]
	s_add_u32 s4, s4, s0
	s_addc_u32 s5, s5, 0
	v_lshl_add_u64 v[68:69], s[4:5], 0, v[210:211]
	global_store_dwordx2 v[68:69], v[70:71], off nt
.Lp7vg_dx:
	s_cmp_lt_i32 s99, 0
	s_cbranch_scc1 .Lp7vg_dy
	s_add_i32 s0, s99, s52
	s_add_i32 s0, s0, 1
	v_pk_mul_f32 v[242:243], v[242:243], s[2:3] op_sel_hi:[1,0]
	v_pk_mul_f32 v[244:245], v[244:245], s[2:3] op_sel_hi:[1,0]
	v_pk_mul_f32 v[246:247], v[246:247], s[2:3] op_sel_hi:[1,0]
	v_pk_mul_f32 v[248:249], v[248:249], s[2:3] op_sel_hi:[1,0]
	s_ashr_i32 s4, s0, 10
	s_ashr_i32 s5, s4, 31
	v_cvt_pk_fp8_f32 v242, v242, v246
	s_lshl_b32 s0, s0, 12
	s_lshl_b64 s[4:5], s[4:5], 22
	v_cvt_pk_fp8_f32 v242, v243, v247 op_sel:[0,0,1]
	s_and_b32 s0, s0, 0x3ff000
	v_readlane_b32 s1, v251, 50
	v_cvt_pk_fp8_f32 v243, v244, v248
	s_add_u32 s4, s1, s4
	v_readlane_b32 s1, v251, 51
	s_addc_u32 s5, s1, s5
	v_cvt_pk_fp8_f32 v243, v245, v249 op_sel:[0,0,1]
	s_add_u32 s4, s4, s0
	s_addc_u32 s5, s5, 0
	v_lshl_add_u64 v[240:241], s[4:5], 0, v[210:211]
	global_store_dwordx2 v[240:241], v[242:243], off nt
.Lp7vg_dy:
.LBB0_810:
	v_readlane_b32 s36, v251, 25
	v_readlane_b32 s39, v251, 28
	v_readlane_b32 s37, v251, 26
	v_readlane_b32 s38, v251, 27
	s_cmp_lt_u32 s39, 9
	s_cbranch_scc1 .LBB0_864
	s_waitcnt vmcnt(0)
	s_barrier
	s_mov_b64 s[0:1], exec
	v_readlane_b32 s2, v251, 23
	v_readlane_b32 s3, v251, 24
	s_and_b64 s[2:3], s[0:1], s[2:3]
	s_mov_b64 exec, s[2:3]
	s_cbranch_execz .LBB0_863
	s_add_u32 s2, s36, 0x4200
	s_addc_u32 s3, s37, 0
	s_add_i32 s4, 0, 0x20160
	v_mov_b32_e32 v1, s4
	s_waitcnt vmcnt(0) expcnt(0) lgkmcnt(0)
	ds_read_b32 v3, v1
	s_add_i32 s4, 0, 0x20164
	v_mov_b32_e32 v1, s4
	ds_read_b32 v1, v1
	s_waitcnt lgkmcnt(1)
	v_cmp_ne_u32_e32 vcc, 0, v3
	s_cbranch_vccnz .LBB0_827
	s_add_u32 s4, s36, 0x4400
	s_addc_u32 s5, s37, 0
	s_add_u32 s8, s36, 0x4500
	s_addc_u32 s9, s37, 0
	s_add_u32 s10, s36, 0x4600
	s_addc_u32 s11, s37, 0
	s_add_u32 s12, s36, 0x4700
	s_addc_u32 s13, s37, 0
	s_add_u32 s14, s36, 0x4800
	s_addc_u32 s15, s37, 0
	s_add_u32 s16, s36, 0x4900
	s_addc_u32 s17, s37, 0
	s_add_u32 s18, s36, 0x4a00
	s_addc_u32 s19, s37, 0
	s_add_u32 s20, s36, 0x4b00
	s_addc_u32 s21, s37, 0
	s_add_u32 s22, s36, 0x4c00
	s_addc_u32 s23, s37, 0
	s_add_u32 s24, s36, 0x4d00
	s_addc_u32 s25, s37, 0
	s_add_u32 s26, s36, 0x4e00
	s_addc_u32 s27, s37, 0
	s_add_u32 s28, s36, 0x4f00
	s_addc_u32 s29, s37, 0
	v_readlane_b32 s42, v251, 0
	s_add_u32 s30, s36, 0x5000
	v_readlane_b32 s43, v251, 1
	s_addc_u32 s31, s37, 0
	s_load_dwordx2 s[40:41], s[42:43], 0x4
	s_add_u32 s34, s36, 0x5100
	s_mov_b64 s[46:47], s[38:39]
	s_addc_u32 s35, s37, 0
	s_mov_b64 s[44:45], s[36:37]
	s_add_u32 s36, s44, 0x5200
	s_addc_u32 s37, s45, 0
	v_readlane_b32 s33, v251, 2
	s_add_u32 s38, s44, 0x5300
	s_waitcnt lgkmcnt(0)
	s_mul_i32 s33, s40, s33
	s_addc_u32 s39, s45, 0
	s_mul_i32 s33, s33, s41
	s_mov_b32 s46, 1
	v_mov_b32_e32 v17, 0
	s_branch .LBB0_815
